# gate/up GEMM unit top: the two compiler VM drains (WAW guard for the bias registers) dropped now that the bias preload is fully drained mid-epilogue; the next unit's slot-list DMA no longer exposes it
# baseline (speedup 1.0000x reference)
;     __device__ __forceinline__ bool next(int i, pg8::Unit& u) const {
;         const int MT = tb[NEXP]; int pm, pn;
;         if (G == 256) { const int x = bx & 7, j = bx >> 3, s = i * 8 + x; pm = s * GM + j / NT; pn = j % NT; }
;         else { const int L = i * G + bx; pm = L / NT; pn = L % NT; }
;         if (pm >= MT) return false;
;         const int e = tb[128 + pm];
;         int rows = tb[40 + e] - 256 * (pm - tb[e]); rows = rows > 256 ? 256 : rows;
;         u.pm = __builtin_amdgcn_readfirstlane(pm); u.pn = __builtin_amdgcn_readfirstlane(pn); u.pb = __builtin_amdgcn_readfirstlane(e * NT + pn); u.aux = __builtin_amdgcn_readfirstlane(e); u.rows = __builtin_amdgcn_readfirstlane(rows); u.lt = __builtin_amdgcn_readfirstlane(pm - tb[e]);
;         return true;
.LBB0_1085:
	s_waitcnt lgkmcnt(0)
	v_cmp_ge_i32_e64 s[4:5], s6, v0
	v_cmp_lt_i32_e64 s[8:9], s6, v0
	s_and_b64 vcc, exec, s[4:5]
	s_mov_b32 s68, s58
	s_mov_b32 s63, s90
	s_cbranch_vccnz .LBB0_1087
	s_lshl_b32 s12, s6, 2
	v_readlane_b32 s2, v253, 53
	s_add_i32 s12, s2, s12
	v_mov_b32_e32 v0, s12
	ds_read_b32 v0, v0 offset:512
	s_ashr_i32 s12, s7, 31
	s_lshr_b32 s12, s12, 29
	s_add_i32 s12, s7, s12
	s_and_b32 s12, s12, -8
	s_waitcnt lgkmcnt(0)
	v_lshlrev_b32_e32 v130, 2, v0
	v_add_u32_e32 v130, s2, v130
	ds_read2_b32 v[130:131], v130 offset1:40
	s_sub_i32 s63, s7, s12
	v_lshlrev_b32_e32 v132, 3, v0
	v_add_u32_e32 v132, s63, v132
	v_readfirstlane_b32 s68, v0
	v_readfirstlane_b32 s36, v132
	s_waitcnt lgkmcnt(0)
	v_subrev_u32_e32 v132, s6, v130
	v_lshlrev_b32_e32 v132, 8, v132
	v_add_u32_e32 v131, v132, v131
	v_min_i32_e32 v131, 0x100, v131
	v_sub_u32_e32 v0, s6, v130
	v_readfirstlane_b32 s92, v131
	v_readfirstlane_b32 s64, v0
	s_mov_b32 s93, s6
	s_mov_b32 s20, s68
	s_mov_b32 s74, s63

; #define PG8_GDMA(u, par) do { int gl_ = lane; asm volatile("" : "+v"(gl_));        \
;         if (wid < 2) __builtin_amdgcn_global_load_lds((const unsigned*)((const char*)gslot + ((size_t)(u).aux * GCAP + (size_t)(u).lt * 256) * 8 + (size_t)(wid * 64 + gl_) * 16), \
;         (PG8_LAS unsigned*)(gtab + (par) * 2048 + wid * 1024), 16, 0, 0); } while (0)
; #define PG8_GREAD(dst, u, par) do { _Pragma("unroll") for (int h_ = 0; h_ < 2; ++h_) _Pragma("unroll") for (int i_ = 0; i_ < 2; ++i_) { const int rl_ = 128 * h_ + grl[i_]; \
;         const int tk_ = *(const PG8_LAS int*)(gtab + (par) * 2048 + rl_ * 8); const unsigned tok_ = (rl_ < (u).rows) ? ((unsigned)tk_ >> 2) : 0u; dst[h_][i_] = tok_ * (unsigned)(K * 2) + gcb[i_]; } } while (0)
; template <class Epi, class Sched, bool ALIGN_EPI = false, bool SP2 = false, bool GATHER = false>
; __device__ __forceinline__ void gemm_phase(PG8_LAS unsigned char* lds, const Gemm g, const Sched& S, const Epi& E, const int2* gslot = nullptr, PG8_LAS unsigned char* gtab = nullptr) {
;     ...
;         if constexpr (GATHER) { if (has_next) PG8_GDMA(nxt, (ui + 1) & 1); }
;         const char* nA = (has_next && !GATHER) ? (const char*)g.A + (size_t)nxt.pm * tstep : cA; const char* nB = has_next ? (const char*)g.Bt + (size_t)nxt.pb * tstep : cB;
;         for (int t = 0; t < nt; t += 2) {
;             const bool last = (t == nt - 2);
;             const char* a1 = cA + (size_t)(t + 1) * kstep;
;             const char* a2 = last ? nA : cA + (size_t)(t + 2) * kstep; const char* b2 = last ? nB : cB + (size_t)(t + 2) * kstep;
;             const char* a3 = a2 + kstep; const char* b3 = b2 + kstep;
;             if (last && has_next) S.a_ready(nxt);
;             if constexpr (GATHER) { if (last) { if (has_next) { PG8_GREAD(vN, nxt, (ui + 1) & 1); } else { _Pragma("unroll") for (int h_ = 0; h_ < 2; ++h_) _Pragma("unroll") for (int i_ = 0; i_ < 2; ++i_) vN[h_][i_] = vC[h_][i_]; } } }
.LBB0_1091:
	s_add_u32 s21, s10, 0x100
	s_addc_u32 s37, s11, 0
	s_lshl_b32 s8, s91, 11
	s_and_b32 s8, s8, 0x800
	s_add_i32 s65, s8, 0
	v_mov_b32_e32 v157, v1
	v_mov_b32_e32 v159, v1
	s_add_i32 s65, s65, 0x21400
	v_cmp_gt_i32_e64 s[8:9], s92, v169
	v_cmp_gt_i32_e64 s[10:11], s92, v171
	v_cmp_gt_i32_e64 s[12:13], s92, v175
	v_cmp_gt_i32_e64 s[14:15], s92, v177
	v_lshl_add_u64 v[130:131], s[30:31], 0, v[158:159]
	v_lshl_add_u64 v[132:133], s[30:31], 0, v[156:157]
	s_mov_b32 s69, -2
	s_mov_b64 s[60:61], 0
	s_branch .LBB0_1094
